# GEMM2 epilogue: the eight per-row gate loads issued together up front (one wait instead of eight)
# baseline (speedup 1.0000x reference)
;     __device__ __forceinline__ void operator()() { if (cnt == turn) run_all(tid_); ++cnt; }
;     __device__ __forceinline__ void operator()(const Acc& acc, const Unit& u, int wr, int wc, int fr, int fq) const {
;         const int row0 = u.pm * BM + wr * 64 + fr, col0 = u.pn * BM + wc * 32 + 8 * fq;
;         f16* Og = O + (size_t)u.g * EROWS * DM;
; #pragma unroll
;         for (int ai = 0; ai < 2; ++ai)
; #pragma unroll
;             for (int m = 0; m < 4; ++m) { const int row = row0 + ai * HALF + m * 16; const float s = gv[((row >> 8) * NE + u.g) * CAP + (row & 255)];
;                 f16* rowp = Og + (size_t)row * DM + col0;
; #pragma unroll
;                 for (int bj = 0; bj < 2; ++bj) { const f32x4 v0 = acc[ai][bj][m][0] * s, v1 = acc[ai][bj][m][1] * s;
;                     u32x4 w; w.x = pkh(v0[0], v0[1]); w.y = pkh(v0[2], v0[3]); w.z = pkh(v1[0], v1[1]); w.w = pkh(v1[2], v1[3]);
;                     *(u32x4*)(rowp + bj * HALF) = w; } }
;     }
.LBB0_1105:
	v_lshl_add_u32 v148, s48, 8, v1
	v_lshrrev_b32_e32 v146, 4, v148
	v_and_b32_e32 v146, 0xfffff0, v146
	v_add_lshl_u32 v166, v146, s18, 8
	v_or_b32_e32 v146, v166, v151
	v_ashrrev_i32_e32 v147, 31, v146
	v_lshl_add_u64 v[146:147], v[146:147], 2, s[72:73]
	global_load_dword v226, v[146:147], off
	global_load_dword v227, v[146:147], off offset:64
	global_load_dword v228, v[146:147], off offset:128
	global_load_dword v229, v[146:147], off offset:192
	global_load_dword v230, v[146:147], off offset:512
	global_load_dword v231, v[146:147], off offset:576
	global_load_dword v232, v[146:147], off offset:640
	global_load_dword v233, v[146:147], off offset:704
	v_lshl_or_b32 v146, s19, 8, v152
	s_ashr_i32 s19, s18, 31
	s_lshl_b64 s[2:3], s[18:19], 23
	s_add_u32 s2, s74, s2
	v_ashrrev_i32_e32 v147, 31, v146
	v_ashrrev_i32_e32 v149, 31, v148
	v_or_b32_e32 v158, 16, v148
	s_addc_u32 s3, s75, s3
	v_lshlrev_b64 v[160:161], 11, v[148:149]
	v_lshl_add_u64 v[146:147], v[146:147], 1, s[2:3]
	v_and_or_b32 v162, v158, s44, v166
	v_lshl_add_u64 v[160:161], v[146:147], 0, v[160:161]
	v_ashrrev_i32_e32 v163, 31, v162
	v_lshl_add_u64 v[162:163], v[162:163], 2, s[72:73]
	v_ashrrev_i32_e32 v159, 31, v158
	s_movk_i32 s2, 0xcf
	s_and_b64 vcc, exec, s[4:5]
	s_waitcnt vmcnt(0)
	v_mov_b32_e32 v156, v226
	v_pk_mul_f32 v[128:129], v[128:129], v[156:157] op_sel_hi:[1,0]
	v_pk_mul_f32 v[126:127], v[126:127], v[156:157] op_sel_hi:[1,0]
	v_pk_mul_f32 v[124:125], v[124:125], v[156:157] op_sel_hi:[1,0]
	v_pk_mul_f32 v[122:123], v[122:123], v[156:157] op_sel_hi:[1,0]
	v_pk_mul_f32 v[120:121], v[120:121], v[156:157] op_sel_hi:[1,0]
	v_pk_mul_f32 v[118:119], v[118:119], v[156:157] op_sel_hi:[1,0]
	v_pk_mul_f32 v[164:165], v[116:117], v[156:157] op_sel_hi:[1,0]
	v_pk_mul_f32 v[156:157], v[114:115], v[156:157] op_sel_hi:[1,0]
	v_cvt_pk_f16_f32 v114, v126, v127
	v_cvt_pk_f16_f32 v115, v128, v129
	v_cvt_pk_f16_f32 v116, v122, v123
	v_cvt_pk_f16_f32 v117, v124, v125
	v_cvt_pk_f16_f32 v118, v118, v119
	v_cvt_pk_f16_f32 v119, v120, v121
	v_cvt_pk_f16_f32 v120, v156, v157
	v_cvt_pk_f16_f32 v121, v164, v165
	global_store_dwordx4 v[160:161], v[114:117], off sc0 sc1
	global_store_dwordx4 v[160:161], v[118:121], off offset:256 sc0 sc1
	s_nop 0
	v_or_b32_e32 v116, 32, v148
	v_lshlrev_b64 v[118:119], 11, v[158:159]
	v_and_or_b32 v120, v116, s45, v166
	v_lshl_add_u64 v[118:119], v[146:147], 0, v[118:119]
	v_ashrrev_i32_e32 v121, 31, v120
	v_lshl_add_u64 v[120:121], v[120:121], 2, s[72:73]
	v_ashrrev_i32_e32 v117, 31, v116
	s_nop 0
	v_mov_b32_e32 v114, v227
	v_pk_mul_f32 v[112:113], v[112:113], v[114:115] op_sel_hi:[1,0]
	v_pk_mul_f32 v[110:111], v[110:111], v[114:115] op_sel_hi:[1,0]
	v_pk_mul_f32 v[108:109], v[108:109], v[114:115] op_sel_hi:[1,0]
	v_pk_mul_f32 v[106:107], v[106:107], v[114:115] op_sel_hi:[1,0]
	v_pk_mul_f32 v[104:105], v[104:105], v[114:115] op_sel_hi:[1,0]
	v_pk_mul_f32 v[102:103], v[102:103], v[114:115] op_sel_hi:[1,0]
	v_pk_mul_f32 v[122:123], v[100:101], v[114:115] op_sel_hi:[1,0]
	v_pk_mul_f32 v[114:115], v[98:99], v[114:115] op_sel_hi:[1,0]
	v_cvt_pk_f16_f32 v98, v110, v111
	v_cvt_pk_f16_f32 v99, v112, v113
	v_cvt_pk_f16_f32 v100, v106, v107
	v_cvt_pk_f16_f32 v101, v108, v109
	v_cvt_pk_f16_f32 v102, v102, v103
	v_cvt_pk_f16_f32 v103, v104, v105
	v_cvt_pk_f16_f32 v104, v114, v115
	v_cvt_pk_f16_f32 v105, v122, v123
	global_store_dwordx4 v[118:119], v[98:101], off sc0 sc1
	global_store_dwordx4 v[118:119], v[102:105], off offset:256 sc0 sc1
	s_nop 0
	v_or_b32_e32 v100, 48, v148
	v_lshlrev_b64 v[102:103], 11, v[116:117]
	v_and_or_b32 v104, v100, s46, v166
	v_lshl_add_u64 v[102:103], v[146:147], 0, v[102:103]
	v_ashrrev_i32_e32 v105, 31, v104
	v_lshl_add_u64 v[104:105], v[104:105], 2, s[72:73]
	v_ashrrev_i32_e32 v101, 31, v100
	s_nop 0
	v_mov_b32_e32 v98, v228
	v_pk_mul_f32 v[96:97], v[96:97], v[98:99] op_sel_hi:[1,0]
	v_pk_mul_f32 v[94:95], v[94:95], v[98:99] op_sel_hi:[1,0]
	v_pk_mul_f32 v[92:93], v[92:93], v[98:99] op_sel_hi:[1,0]
	v_pk_mul_f32 v[90:91], v[90:91], v[98:99] op_sel_hi:[1,0]
	v_pk_mul_f32 v[88:89], v[88:89], v[98:99] op_sel_hi:[1,0]
	v_pk_mul_f32 v[86:87], v[86:87], v[98:99] op_sel_hi:[1,0]
	v_pk_mul_f32 v[106:107], v[84:85], v[98:99] op_sel_hi:[1,0]
	v_pk_mul_f32 v[98:99], v[82:83], v[98:99] op_sel_hi:[1,0]
	v_cvt_pk_f16_f32 v82, v94, v95
	v_cvt_pk_f16_f32 v83, v96, v97
	v_cvt_pk_f16_f32 v84, v90, v91
	v_cvt_pk_f16_f32 v85, v92, v93
	v_cvt_pk_f16_f32 v86, v86, v87
	v_cvt_pk_f16_f32 v87, v88, v89
	v_cvt_pk_f16_f32 v88, v98, v99
	v_cvt_pk_f16_f32 v89, v106, v107
	global_store_dwordx4 v[102:103], v[82:85], off sc0 sc1
	global_store_dwordx4 v[102:103], v[86:89], off offset:256 sc0 sc1
	s_nop 0
	v_add_u32_e32 v84, 0x80, v148
	v_lshrrev_b32_e32 v83, 4, v84
	v_and_b32_e32 v83, 0xfffff0, v83
	v_add_lshl_u32 v92, v83, s18, 8
	v_lshlrev_b64 v[86:87], 11, v[100:101]
	v_and_or_b32 v88, v84, s2, v92
	v_lshl_add_u64 v[86:87], v[146:147], 0, v[86:87]
	v_ashrrev_i32_e32 v89, 31, v88
	v_lshl_add_u64 v[88:89], v[88:89], 2, s[72:73]
	v_ashrrev_i32_e32 v85, 31, v84
	s_mov_b64 s[2:3], -1
	s_nop 0
	v_mov_b32_e32 v82, v229
	v_pk_mul_f32 v[80:81], v[80:81], v[82:83] op_sel_hi:[1,0]
	v_pk_mul_f32 v[78:79], v[78:79], v[82:83] op_sel_hi:[1,0]
;     __device__ __forceinline__ void operator()(const Acc& acc, const Unit& u, int wr, int wc, int fr, int fq) const {
;     ...
;             for (int m = 0; m < 4; ++m) { const int row = row0 + ai * HALF + m * 16; const float s = gv[((row >> 8) * NE + u.g) * CAP + (row & 255)];
;                 f16* rowp = Og + (size_t)row * DM + col0;
; #pragma unroll
;                 for (int bj = 0; bj < 2; ++bj) { const f32x4 v0 = acc[ai][bj][m][0] * s, v1 = acc[ai][bj][m][1] * s;
;                     u32x4 w; w.x = pkh(v0[0], v0[1]); w.y = pkh(v0[2], v0[3]); w.z = pkh(v1[0], v1[1]); w.w = pkh(v1[2], v1[3]);
;                     *(u32x4*)(rowp + bj * HALF) = w; } }
;     }
	v_pk_mul_f32 v[76:77], v[76:77], v[82:83] op_sel_hi:[1,0]
	v_pk_mul_f32 v[74:75], v[74:75], v[82:83] op_sel_hi:[1,0]
	v_pk_mul_f32 v[72:73], v[72:73], v[82:83] op_sel_hi:[1,0]
	v_pk_mul_f32 v[70:71], v[70:71], v[82:83] op_sel_hi:[1,0]
	v_pk_mul_f32 v[90:91], v[68:69], v[82:83] op_sel_hi:[1,0]
	v_pk_mul_f32 v[82:83], v[66:67], v[82:83] op_sel_hi:[1,0]
	v_cvt_pk_f16_f32 v66, v78, v79
	v_cvt_pk_f16_f32 v67, v80, v81
	v_cvt_pk_f16_f32 v68, v74, v75
	v_cvt_pk_f16_f32 v69, v76, v77
	v_cvt_pk_f16_f32 v70, v70, v71
	v_cvt_pk_f16_f32 v71, v72, v73
	v_cvt_pk_f16_f32 v72, v82, v83
	v_cvt_pk_f16_f32 v73, v90, v91
	global_store_dwordx4 v[86:87], v[66:69], off sc0 sc1
	global_store_dwordx4 v[86:87], v[70:73], off offset:256 sc0 sc1
	s_nop 0
	v_add_u32_e32 v68, 0x90, v148
	v_lshlrev_b64 v[70:71], 11, v[84:85]
	v_and_or_b32 v72, v68, s44, v92
	v_lshl_add_u64 v[70:71], v[146:147], 0, v[70:71]
	v_ashrrev_i32_e32 v73, 31, v72
	v_lshl_add_u64 v[72:73], v[72:73], 2, s[72:73]
	v_ashrrev_i32_e32 v69, 31, v68
	s_nop 0
	v_mov_b32_e32 v66, v230
	v_pk_mul_f32 v[64:65], v[64:65], v[66:67] op_sel_hi:[1,0]
	v_pk_mul_f32 v[62:63], v[62:63], v[66:67] op_sel_hi:[1,0]
	v_pk_mul_f32 v[60:61], v[60:61], v[66:67] op_sel_hi:[1,0]
	v_pk_mul_f32 v[58:59], v[58:59], v[66:67] op_sel_hi:[1,0]
	v_pk_mul_f32 v[56:57], v[56:57], v[66:67] op_sel_hi:[1,0]
	v_pk_mul_f32 v[54:55], v[54:55], v[66:67] op_sel_hi:[1,0]
	v_pk_mul_f32 v[74:75], v[52:53], v[66:67] op_sel_hi:[1,0]
	v_pk_mul_f32 v[66:67], v[50:51], v[66:67] op_sel_hi:[1,0]
	v_cvt_pk_f16_f32 v50, v62, v63
	v_cvt_pk_f16_f32 v51, v64, v65
	v_cvt_pk_f16_f32 v52, v58, v59
	v_cvt_pk_f16_f32 v53, v60, v61
	v_cvt_pk_f16_f32 v54, v54, v55
	v_cvt_pk_f16_f32 v55, v56, v57
	v_cvt_pk_f16_f32 v56, v66, v67
	v_cvt_pk_f16_f32 v57, v74, v75
	global_store_dwordx4 v[70:71], v[50:53], off sc0 sc1
	global_store_dwordx4 v[70:71], v[54:57], off offset:256 sc0 sc1
	s_nop 0
	v_add_u32_e32 v52, 0xa0, v148
	v_lshlrev_b64 v[54:55], 11, v[68:69]
	v_and_or_b32 v56, v52, s45, v92
	v_lshl_add_u64 v[54:55], v[146:147], 0, v[54:55]
	v_ashrrev_i32_e32 v57, 31, v56
	v_lshl_add_u64 v[56:57], v[56:57], 2, s[72:73]
	v_ashrrev_i32_e32 v53, 31, v52
	s_nop 0
	v_mov_b32_e32 v50, v231
	v_pk_mul_f32 v[48:49], v[48:49], v[50:51] op_sel_hi:[1,0]
	v_pk_mul_f32 v[46:47], v[46:47], v[50:51] op_sel_hi:[1,0]
	v_pk_mul_f32 v[44:45], v[44:45], v[50:51] op_sel_hi:[1,0]
	v_pk_mul_f32 v[42:43], v[42:43], v[50:51] op_sel_hi:[1,0]
	v_pk_mul_f32 v[40:41], v[40:41], v[50:51] op_sel_hi:[1,0]
	v_pk_mul_f32 v[38:39], v[38:39], v[50:51] op_sel_hi:[1,0]
	v_pk_mul_f32 v[58:59], v[36:37], v[50:51] op_sel_hi:[1,0]
	v_pk_mul_f32 v[50:51], v[34:35], v[50:51] op_sel_hi:[1,0]
	v_cvt_pk_f16_f32 v34, v46, v47
	v_cvt_pk_f16_f32 v35, v48, v49
	v_cvt_pk_f16_f32 v36, v42, v43
	v_cvt_pk_f16_f32 v37, v44, v45
	v_cvt_pk_f16_f32 v38, v38, v39
	v_cvt_pk_f16_f32 v39, v40, v41
	v_cvt_pk_f16_f32 v40, v50, v51
	v_cvt_pk_f16_f32 v41, v58, v59
	global_store_dwordx4 v[54:55], v[34:37], off sc0 sc1
	global_store_dwordx4 v[54:55], v[38:41], off offset:256 sc0 sc1
	s_nop 0
	v_add_u32_e32 v36, 0xb0, v148
	v_lshlrev_b64 v[38:39], 11, v[52:53]
	v_and_or_b32 v40, v36, s46, v92
	v_lshl_add_u64 v[38:39], v[146:147], 0, v[38:39]
	v_ashrrev_i32_e32 v41, 31, v40
	v_lshl_add_u64 v[40:41], v[40:41], 2, s[72:73]
	v_ashrrev_i32_e32 v37, 31, v36
	s_nop 0
	v_mov_b32_e32 v34, v232
	v_pk_mul_f32 v[32:33], v[32:33], v[34:35] op_sel_hi:[1,0]
	v_pk_mul_f32 v[30:31], v[30:31], v[34:35] op_sel_hi:[1,0]
	v_pk_mul_f32 v[28:29], v[28:29], v[34:35] op_sel_hi:[1,0]
	v_pk_mul_f32 v[26:27], v[26:27], v[34:35] op_sel_hi:[1,0]
	v_pk_mul_f32 v[24:25], v[24:25], v[34:35] op_sel_hi:[1,0]
	v_pk_mul_f32 v[22:23], v[22:23], v[34:35] op_sel_hi:[1,0]
	v_pk_mul_f32 v[42:43], v[20:21], v[34:35] op_sel_hi:[1,0]
	v_pk_mul_f32 v[34:35], v[18:19], v[34:35] op_sel_hi:[1,0]
	v_cvt_pk_f16_f32 v18, v30, v31
	v_cvt_pk_f16_f32 v19, v32, v33
	v_cvt_pk_f16_f32 v20, v26, v27
	v_cvt_pk_f16_f32 v21, v28, v29
	v_cvt_pk_f16_f32 v22, v22, v23
	v_cvt_pk_f16_f32 v23, v24, v25
	v_cvt_pk_f16_f32 v24, v34, v35
	v_cvt_pk_f16_f32 v25, v42, v43
	global_store_dwordx4 v[38:39], v[18:21], off sc0 sc1
	global_store_dwordx4 v[38:39], v[22:25], off offset:256 sc0 sc1
	s_nop 0
	v_lshlrev_b64 v[20:21], 11, v[36:37]
	v_lshl_add_u64 v[20:21], v[146:147], 0, v[20:21]
	s_nop 0
	v_mov_b32_e32 v18, v233
	v_pk_mul_f32 v[16:17], v[16:17], v[18:19] op_sel_hi:[1,0]
	v_pk_mul_f32 v[14:15], v[14:15], v[18:19] op_sel_hi:[1,0]
	v_pk_mul_f32 v[12:13], v[12:13], v[18:19] op_sel_hi:[1,0]
	v_pk_mul_f32 v[10:11], v[10:11], v[18:19] op_sel_hi:[1,0]
	v_pk_mul_f32 v[8:9], v[8:9], v[18:19] op_sel_hi:[1,0]
	v_pk_mul_f32 v[6:7], v[6:7], v[18:19] op_sel_hi:[1,0]
	v_pk_mul_f32 v[22:23], v[4:5], v[18:19] op_sel_hi:[1,0]
	v_pk_mul_f32 v[18:19], v[2:3], v[18:19] op_sel_hi:[1,0]
	v_cvt_pk_f16_f32 v2, v14, v15
	v_cvt_pk_f16_f32 v3, v16, v17
	v_cvt_pk_f16_f32 v4, v10, v11
	v_cvt_pk_f16_f32 v5, v12, v13
	v_cvt_pk_f16_f32 v6, v6, v7
	v_cvt_pk_f16_f32 v7, v8, v9
	v_cvt_pk_f16_f32 v8, v18, v19
	v_cvt_pk_f16_f32 v9, v22, v23
	global_store_dwordx4 v[20:21], v[2:5], off sc0 sc1
	global_store_dwordx4 v[20:21], v[6:9], off offset:256 sc0 sc1
	s_cbranch_vccnz .LBB0_1087
	s_andn2_b64 vcc, exec, s[10:11]
	s_cbranch_vccnz .LBB0_1086
	s_barrier
	s_branch .LBB0_1086

;     __device__ __forceinline__ void operator()() { if (cnt == turn) run_all(tid_); ++cnt; }
;     __device__ __forceinline__ void operator()(const Acc& acc, const Unit& u, int wr, int wc, int fr, int fq) const {
;         const int row0 = u.pm * BM + wr * 64 + fr, col0 = u.pn * BM + wc * 32 + 8 * fq;
;         f16* Og = O + (size_t)u.g * EROWS * DM;
; #pragma unroll
;         for (int ai = 0; ai < 2; ++ai)
; #pragma unroll
;             for (int m = 0; m < 4; ++m) { const int row = row0 + ai * HALF + m * 16; const float s = gv[((row >> 8) * NE + u.g) * CAP + (row & 255)];
;                 f16* rowp = Og + (size_t)row * DM + col0;
; #pragma unroll
;                 for (int bj = 0; bj < 2; ++bj) { const f32x4 v0 = acc[ai][bj][m][0] * s, v1 = acc[ai][bj][m][1] * s;
;                     u32x4 w; w.x = pkh(v0[0], v0[1]); w.y = pkh(v0[2], v0[3]); w.z = pkh(v1[0], v1[1]); w.w = pkh(v1[2], v1[3]);
;                     *(u32x4*)(rowp + bj * HALF) = w; } }
;     }
.LBB0_1870:
	v_lshl_add_u32 v148, s49, 8, v1
	v_lshrrev_b32_e32 v146, 4, v148
	v_and_b32_e32 v146, 0xfffff0, v146
	v_add_lshl_u32 v166, v146, s16, 8
	v_or_b32_e32 v146, v166, v151
	v_ashrrev_i32_e32 v147, 31, v146
	v_lshl_add_u64 v[146:147], v[146:147], 2, s[72:73]
	global_load_dword v226, v[146:147], off
	global_load_dword v227, v[146:147], off offset:64
	global_load_dword v228, v[146:147], off offset:128
	global_load_dword v229, v[146:147], off offset:192
	global_load_dword v230, v[146:147], off offset:512
	global_load_dword v231, v[146:147], off offset:576
	global_load_dword v232, v[146:147], off offset:640
	global_load_dword v233, v[146:147], off offset:704
	v_lshl_or_b32 v146, s17, 8, v152
	s_ashr_i32 s17, s16, 31
	s_lshl_b64 s[2:3], s[16:17], 23
	s_add_u32 s2, s74, s2
	v_ashrrev_i32_e32 v147, 31, v146
	v_ashrrev_i32_e32 v149, 31, v148
	v_or_b32_e32 v158, 16, v148
	s_addc_u32 s3, s75, s3
	v_lshlrev_b64 v[160:161], 11, v[148:149]
	v_lshl_add_u64 v[146:147], v[146:147], 1, s[2:3]
	v_and_or_b32 v162, v158, s45, v166
	v_lshl_add_u64 v[160:161], v[146:147], 0, v[160:161]
	v_ashrrev_i32_e32 v163, 31, v162
	v_lshl_add_u64 v[162:163], v[162:163], 2, s[72:73]
	v_ashrrev_i32_e32 v159, 31, v158
	s_and_b64 vcc, exec, s[4:5]
	s_mov_b64 s[2:3], -1
	s_waitcnt vmcnt(0)
	v_mov_b32_e32 v156, v226
	v_pk_mul_f32 v[128:129], v[128:129], v[156:157] op_sel_hi:[1,0]
	v_pk_mul_f32 v[126:127], v[126:127], v[156:157] op_sel_hi:[1,0]
	v_pk_mul_f32 v[124:125], v[124:125], v[156:157] op_sel_hi:[1,0]
	v_pk_mul_f32 v[122:123], v[122:123], v[156:157] op_sel_hi:[1,0]
	v_pk_mul_f32 v[120:121], v[120:121], v[156:157] op_sel_hi:[1,0]
	v_pk_mul_f32 v[118:119], v[118:119], v[156:157] op_sel_hi:[1,0]
	v_pk_mul_f32 v[164:165], v[116:117], v[156:157] op_sel_hi:[1,0]
	v_pk_mul_f32 v[156:157], v[114:115], v[156:157] op_sel_hi:[1,0]
	v_cvt_pk_f16_f32 v114, v126, v127
	v_cvt_pk_f16_f32 v115, v128, v129
	v_cvt_pk_f16_f32 v116, v122, v123
	v_cvt_pk_f16_f32 v117, v124, v125
	v_cvt_pk_f16_f32 v118, v118, v119
	v_cvt_pk_f16_f32 v119, v120, v121
	v_cvt_pk_f16_f32 v120, v156, v157
	v_cvt_pk_f16_f32 v121, v164, v165
	global_store_dwordx4 v[160:161], v[114:117], off sc0 sc1
	global_store_dwordx4 v[160:161], v[118:121], off offset:256 sc0 sc1
	s_nop 0
	v_or_b32_e32 v116, 32, v148
	v_lshlrev_b64 v[118:119], 11, v[158:159]
	v_and_or_b32 v120, v116, s46, v166
	v_lshl_add_u64 v[118:119], v[146:147], 0, v[118:119]
	v_ashrrev_i32_e32 v121, 31, v120
	v_lshl_add_u64 v[120:121], v[120:121], 2, s[72:73]
	v_ashrrev_i32_e32 v117, 31, v116
	s_nop 0
	v_mov_b32_e32 v114, v227
	v_pk_mul_f32 v[112:113], v[112:113], v[114:115] op_sel_hi:[1,0]
	v_pk_mul_f32 v[110:111], v[110:111], v[114:115] op_sel_hi:[1,0]
	v_pk_mul_f32 v[108:109], v[108:109], v[114:115] op_sel_hi:[1,0]
	v_pk_mul_f32 v[106:107], v[106:107], v[114:115] op_sel_hi:[1,0]
	v_pk_mul_f32 v[104:105], v[104:105], v[114:115] op_sel_hi:[1,0]
	v_pk_mul_f32 v[102:103], v[102:103], v[114:115] op_sel_hi:[1,0]
	v_pk_mul_f32 v[122:123], v[100:101], v[114:115] op_sel_hi:[1,0]
	v_pk_mul_f32 v[114:115], v[98:99], v[114:115] op_sel_hi:[1,0]
	v_cvt_pk_f16_f32 v98, v110, v111
	v_cvt_pk_f16_f32 v99, v112, v113
	v_cvt_pk_f16_f32 v100, v106, v107
	v_cvt_pk_f16_f32 v101, v108, v109
	v_cvt_pk_f16_f32 v102, v102, v103
	v_cvt_pk_f16_f32 v103, v104, v105
	v_cvt_pk_f16_f32 v104, v114, v115
	v_cvt_pk_f16_f32 v105, v122, v123
	global_store_dwordx4 v[118:119], v[98:101], off sc0 sc1
	global_store_dwordx4 v[118:119], v[102:105], off offset:256 sc0 sc1
	s_nop 0
	v_or_b32_e32 v100, 48, v148
	v_lshlrev_b64 v[102:103], 11, v[116:117]
	v_and_or_b32 v104, v100, s47, v166
	v_lshl_add_u64 v[102:103], v[146:147], 0, v[102:103]
	v_ashrrev_i32_e32 v105, 31, v104
	v_lshl_add_u64 v[104:105], v[104:105], 2, s[72:73]
	v_ashrrev_i32_e32 v101, 31, v100
	s_nop 0
	v_mov_b32_e32 v98, v228
	v_pk_mul_f32 v[96:97], v[96:97], v[98:99] op_sel_hi:[1,0]
	v_pk_mul_f32 v[94:95], v[94:95], v[98:99] op_sel_hi:[1,0]
	v_pk_mul_f32 v[92:93], v[92:93], v[98:99] op_sel_hi:[1,0]
	v_pk_mul_f32 v[90:91], v[90:91], v[98:99] op_sel_hi:[1,0]
	v_pk_mul_f32 v[88:89], v[88:89], v[98:99] op_sel_hi:[1,0]
	v_pk_mul_f32 v[86:87], v[86:87], v[98:99] op_sel_hi:[1,0]
	v_pk_mul_f32 v[106:107], v[84:85], v[98:99] op_sel_hi:[1,0]
	v_pk_mul_f32 v[98:99], v[82:83], v[98:99] op_sel_hi:[1,0]
	v_cvt_pk_f16_f32 v82, v94, v95
	v_cvt_pk_f16_f32 v83, v96, v97
	v_cvt_pk_f16_f32 v84, v90, v91
	v_cvt_pk_f16_f32 v85, v92, v93
	v_cvt_pk_f16_f32 v86, v86, v87
	v_cvt_pk_f16_f32 v87, v88, v89
	v_cvt_pk_f16_f32 v88, v98, v99
	v_cvt_pk_f16_f32 v89, v106, v107
	global_store_dwordx4 v[102:103], v[82:85], off sc0 sc1
	global_store_dwordx4 v[102:103], v[86:89], off offset:256 sc0 sc1
	s_nop 0
	v_add_u32_e32 v84, 0x80, v148
	v_lshrrev_b32_e32 v83, 4, v84
	v_and_b32_e32 v83, 0xfffff0, v83
	v_add_lshl_u32 v92, v83, s16, 8
	v_lshlrev_b64 v[86:87], 11, v[100:101]
	v_and_or_b32 v88, v84, s38, v92
	v_lshl_add_u64 v[86:87], v[146:147], 0, v[86:87]
	v_ashrrev_i32_e32 v89, 31, v88
	v_lshl_add_u64 v[88:89], v[88:89], 2, s[72:73]
	v_ashrrev_i32_e32 v85, 31, v84
	s_nop 0
	v_mov_b32_e32 v82, v229
	v_pk_mul_f32 v[80:81], v[80:81], v[82:83] op_sel_hi:[1,0]
	v_pk_mul_f32 v[78:79], v[78:79], v[82:83] op_sel_hi:[1,0]
	v_pk_mul_f32 v[76:77], v[76:77], v[82:83] op_sel_hi:[1,0]
;     __device__ __forceinline__ void operator()(const Acc& acc, const Unit& u, int wr, int wc, int fr, int fq) const {
;     ...
;             for (int m = 0; m < 4; ++m) { const int row = row0 + ai * HALF + m * 16; const float s = gv[((row >> 8) * NE + u.g) * CAP + (row & 255)];
;                 f16* rowp = Og + (size_t)row * DM + col0;
; #pragma unroll
;                 for (int bj = 0; bj < 2; ++bj) { const f32x4 v0 = acc[ai][bj][m][0] * s, v1 = acc[ai][bj][m][1] * s;
;                     u32x4 w; w.x = pkh(v0[0], v0[1]); w.y = pkh(v0[2], v0[3]); w.z = pkh(v1[0], v1[1]); w.w = pkh(v1[2], v1[3]);
;                     *(u32x4*)(rowp + bj * HALF) = w; } }
;     }
	v_pk_mul_f32 v[74:75], v[74:75], v[82:83] op_sel_hi:[1,0]
	v_pk_mul_f32 v[72:73], v[72:73], v[82:83] op_sel_hi:[1,0]
	v_pk_mul_f32 v[70:71], v[70:71], v[82:83] op_sel_hi:[1,0]
	v_pk_mul_f32 v[90:91], v[68:69], v[82:83] op_sel_hi:[1,0]
	v_pk_mul_f32 v[82:83], v[66:67], v[82:83] op_sel_hi:[1,0]
	v_cvt_pk_f16_f32 v66, v78, v79
	v_cvt_pk_f16_f32 v67, v80, v81
	v_cvt_pk_f16_f32 v68, v74, v75
	v_cvt_pk_f16_f32 v69, v76, v77
	v_cvt_pk_f16_f32 v70, v70, v71
	v_cvt_pk_f16_f32 v71, v72, v73
	v_cvt_pk_f16_f32 v72, v82, v83
	v_cvt_pk_f16_f32 v73, v90, v91
	global_store_dwordx4 v[86:87], v[66:69], off sc0 sc1
	global_store_dwordx4 v[86:87], v[70:73], off offset:256 sc0 sc1
	s_nop 0
	v_add_u32_e32 v68, 0x90, v148
	v_lshlrev_b64 v[70:71], 11, v[84:85]
	v_and_or_b32 v72, v68, s45, v92
	v_lshl_add_u64 v[70:71], v[146:147], 0, v[70:71]
	v_ashrrev_i32_e32 v73, 31, v72
	v_lshl_add_u64 v[72:73], v[72:73], 2, s[72:73]
	v_ashrrev_i32_e32 v69, 31, v68
	s_nop 0
	v_mov_b32_e32 v66, v230
	v_pk_mul_f32 v[64:65], v[64:65], v[66:67] op_sel_hi:[1,0]
	v_pk_mul_f32 v[62:63], v[62:63], v[66:67] op_sel_hi:[1,0]
	v_pk_mul_f32 v[60:61], v[60:61], v[66:67] op_sel_hi:[1,0]
	v_pk_mul_f32 v[58:59], v[58:59], v[66:67] op_sel_hi:[1,0]
	v_pk_mul_f32 v[56:57], v[56:57], v[66:67] op_sel_hi:[1,0]
	v_pk_mul_f32 v[54:55], v[54:55], v[66:67] op_sel_hi:[1,0]
	v_pk_mul_f32 v[74:75], v[52:53], v[66:67] op_sel_hi:[1,0]
	v_pk_mul_f32 v[66:67], v[50:51], v[66:67] op_sel_hi:[1,0]
	v_cvt_pk_f16_f32 v50, v62, v63
	v_cvt_pk_f16_f32 v51, v64, v65
	v_cvt_pk_f16_f32 v52, v58, v59
	v_cvt_pk_f16_f32 v53, v60, v61
	v_cvt_pk_f16_f32 v54, v54, v55
	v_cvt_pk_f16_f32 v55, v56, v57
	v_cvt_pk_f16_f32 v56, v66, v67
	v_cvt_pk_f16_f32 v57, v74, v75
	global_store_dwordx4 v[70:71], v[50:53], off sc0 sc1
	global_store_dwordx4 v[70:71], v[54:57], off offset:256 sc0 sc1
	s_nop 0
	v_add_u32_e32 v52, 0xa0, v148
	v_lshlrev_b64 v[54:55], 11, v[68:69]
	v_and_or_b32 v56, v52, s46, v92
	v_lshl_add_u64 v[54:55], v[146:147], 0, v[54:55]
	v_ashrrev_i32_e32 v57, 31, v56
	v_lshl_add_u64 v[56:57], v[56:57], 2, s[72:73]
	v_ashrrev_i32_e32 v53, 31, v52
	s_nop 0
	v_mov_b32_e32 v50, v231
	v_pk_mul_f32 v[48:49], v[48:49], v[50:51] op_sel_hi:[1,0]
	v_pk_mul_f32 v[46:47], v[46:47], v[50:51] op_sel_hi:[1,0]
	v_pk_mul_f32 v[44:45], v[44:45], v[50:51] op_sel_hi:[1,0]
	v_pk_mul_f32 v[42:43], v[42:43], v[50:51] op_sel_hi:[1,0]
	v_pk_mul_f32 v[40:41], v[40:41], v[50:51] op_sel_hi:[1,0]
	v_pk_mul_f32 v[38:39], v[38:39], v[50:51] op_sel_hi:[1,0]
	v_pk_mul_f32 v[58:59], v[36:37], v[50:51] op_sel_hi:[1,0]
	v_pk_mul_f32 v[50:51], v[34:35], v[50:51] op_sel_hi:[1,0]
	v_cvt_pk_f16_f32 v34, v46, v47
	v_cvt_pk_f16_f32 v35, v48, v49
	v_cvt_pk_f16_f32 v36, v42, v43
	v_cvt_pk_f16_f32 v37, v44, v45
	v_cvt_pk_f16_f32 v38, v38, v39
	v_cvt_pk_f16_f32 v39, v40, v41
	v_cvt_pk_f16_f32 v40, v50, v51
	v_cvt_pk_f16_f32 v41, v58, v59
	global_store_dwordx4 v[54:55], v[34:37], off sc0 sc1
	global_store_dwordx4 v[54:55], v[38:41], off offset:256 sc0 sc1
	s_nop 0
	v_add_u32_e32 v36, 0xb0, v148
	v_lshlrev_b64 v[38:39], 11, v[52:53]
	v_and_or_b32 v40, v36, s47, v92
	v_lshl_add_u64 v[38:39], v[146:147], 0, v[38:39]
	v_ashrrev_i32_e32 v41, 31, v40
	v_lshl_add_u64 v[40:41], v[40:41], 2, s[72:73]
	v_ashrrev_i32_e32 v37, 31, v36
	s_nop 0
	v_mov_b32_e32 v34, v232
	v_pk_mul_f32 v[32:33], v[32:33], v[34:35] op_sel_hi:[1,0]
	v_pk_mul_f32 v[30:31], v[30:31], v[34:35] op_sel_hi:[1,0]
	v_pk_mul_f32 v[28:29], v[28:29], v[34:35] op_sel_hi:[1,0]
	v_pk_mul_f32 v[26:27], v[26:27], v[34:35] op_sel_hi:[1,0]
	v_pk_mul_f32 v[24:25], v[24:25], v[34:35] op_sel_hi:[1,0]
	v_pk_mul_f32 v[22:23], v[22:23], v[34:35] op_sel_hi:[1,0]
	v_pk_mul_f32 v[42:43], v[20:21], v[34:35] op_sel_hi:[1,0]
	v_pk_mul_f32 v[34:35], v[18:19], v[34:35] op_sel_hi:[1,0]
	v_cvt_pk_f16_f32 v18, v30, v31
	v_cvt_pk_f16_f32 v19, v32, v33
	v_cvt_pk_f16_f32 v20, v26, v27
	v_cvt_pk_f16_f32 v21, v28, v29
	v_cvt_pk_f16_f32 v22, v22, v23
	v_cvt_pk_f16_f32 v23, v24, v25
	v_cvt_pk_f16_f32 v24, v34, v35
	v_cvt_pk_f16_f32 v25, v42, v43
	global_store_dwordx4 v[38:39], v[18:21], off sc0 sc1
	global_store_dwordx4 v[38:39], v[22:25], off offset:256 sc0 sc1
	s_nop 0
	v_lshlrev_b64 v[20:21], 11, v[36:37]
	v_lshl_add_u64 v[20:21], v[146:147], 0, v[20:21]
	s_nop 0
	v_mov_b32_e32 v18, v233
	v_pk_mul_f32 v[16:17], v[16:17], v[18:19] op_sel_hi:[1,0]
	v_pk_mul_f32 v[14:15], v[14:15], v[18:19] op_sel_hi:[1,0]
	v_pk_mul_f32 v[12:13], v[12:13], v[18:19] op_sel_hi:[1,0]
	v_pk_mul_f32 v[10:11], v[10:11], v[18:19] op_sel_hi:[1,0]
	v_pk_mul_f32 v[8:9], v[8:9], v[18:19] op_sel_hi:[1,0]
	v_pk_mul_f32 v[6:7], v[6:7], v[18:19] op_sel_hi:[1,0]
	v_pk_mul_f32 v[22:23], v[4:5], v[18:19] op_sel_hi:[1,0]
	v_pk_mul_f32 v[18:19], v[2:3], v[18:19] op_sel_hi:[1,0]
	v_cvt_pk_f16_f32 v2, v14, v15
	v_cvt_pk_f16_f32 v3, v16, v17
	v_cvt_pk_f16_f32 v4, v10, v11
	v_cvt_pk_f16_f32 v5, v12, v13
	v_cvt_pk_f16_f32 v6, v6, v7
	v_cvt_pk_f16_f32 v7, v8, v9
	v_cvt_pk_f16_f32 v8, v18, v19
	v_cvt_pk_f16_f32 v9, v22, v23
	global_store_dwordx4 v[20:21], v[2:5], off sc0 sc1
	global_store_dwordx4 v[20:21], v[6:9], off offset:256 sc0 sc1
	s_cbranch_vccnz .LBB0_1852
	s_andn2_b64 vcc, exec, s[10:11]
	s_cbranch_vccnz .LBB0_1851
	s_barrier
	s_branch .LBB0_1851
